# attention LDS-DMA pieces no longer save and restore M0 (no consumer of a preserved M0 exists): 28 scalar moves removed and no M0 write behind the second piece
# speedup vs baseline: 1.0038x; 1.0038x over previous
; #define WAIT_BAR(N) asm volatile("s_waitcnt vmcnt(" #N ") lgkmcnt(0)\n\ts_barrier":::"memory")
;   #define DMA_K(t,slot) glds16(ksrc+(long)(t)*KVBLK*DM,(unsigned)__builtin_amdgcn_readfirstlane(kdst+(slot)))
;   #define DMA_V(t,slot) glds16(vsrc+(long)(t)*KVBLK*DM,(unsigned)__builtin_amdgcn_readfirstlane(vdst+(slot)))
;   #define WLOAD(W,t) asm volatile("global_load_dword %0, %1, off":"=v"(W):"v"(mwl+(size_t)(t)*64):"memory")
; template<int THRL> __device__ __forceinline__ void attn_unit(int b,int h,int qb,const bf16*Q,const bf16*__restrict__ K,const bf16*__restrict__ V,bf16*O,const unsigned*MASK,char*shm){
;   int tid_=threadIdx.x; asm volatile("":"+v"(tid_));
;   const int tid=tid_,lane=tid&63,r32=lane&31,hi=lane>>5; const int wid=__builtin_amdgcn_readfirstlane(tid>>6);
;   const long rowbase=(long)b*SEQ; const int q0=qb*QB;
;   const bf16*Qw=Q+(rowbase+q0+wid*QBLK)*DM+h*D;
;   const bf16*Kh=K+rowbase*DM+h*D,*Vh=V+rowbase*DM+h*D;
;   const unsigned lds0=(unsigned)(uintptr_t)shm;
;   float*wsf=(float*)(shm+LDS_WS)+wid*64;
;   const bf16*ksrc=Kh+(long)lane*DM+wid*8;
;   const bf16*vsrc=Vh+(long)(16*(wid&3)+(lane>>2))*DM+(wid>>2)*32+(lane&3)*8;
;   const unsigned kdst=lds0+LDS_K+wid*1024, vdst=lds0+LDS_V+wid*1024;
;     ...
;   const int vb0=(int)(lds0+LDS_V)+((lane>>4)&1)*32+(lane&3)*8+(4*hi+((lane&15)>>2))*64;
;   const char*Kbase=shm+LDS_K; bf16x8 kf[8];
;   const lds_cptr shm3=(lds_cptr)shm; const lds_cptr kp0=shm3+LDS_K+hi*1024+r32*16; const lds_cptr vp0=shm3+LDS_V+((lane>>4)&1)*32+(lane&3)*8+(4*hi+((lane&15)>>2))*64;
;   const int NT=(q0+QB)/KVBLK;
;   const unsigned*mwl=MASK+((size_t)(b*256+qb*8+wid)*128)*64+lane;
;   unsigned wA,wB;
;     ...
;   WLOAD(wA,0);WLOAD(wB,1);
;   DMA_K(0,0);DMA_V(0,0);DMA_K(1,SLOTB);
;   bf16x8 qr[4];
;   #pragma unroll
;   for(int d0=0;d0<4;++d0)qr[d0]=*reinterpret_cast<const bf16x8*>(&Qw[(long)r32*DM+d0*16+hi*8]);
;   float mhat=0.f,l_reg=0.f;f32x16 o[2];o[0]=f32x16{};o[1]=f32x16{};f32x16 negm=f32x16{};asm volatile("":"+v"(negm));
;   bool resc=false;
;     ...
;   f32x16 pA0,pA1,pB0,pB1;
;   int sl_prev=0,sl_cur=0,sl_next=SLOTB;
;     ...
;   DMA_K(2,2*SLOTB);
;   WAIT_BAR(3);
.LBB0_1271:
	s_ashr_i32 s4, s6, 31
	s_lshr_b32 s4, s4, 29
	s_add_i32 s4, s6, s4
	s_ashr_i32 s42, s4, 3
	v_mov_b32_e32 v58, v0
	s_and_b32 s4, s4, 0x3fffff8
	s_ashr_i32 s43, s42, 31
	v_readfirstlane_b32 s50, v58
	s_lshl_b32 s51, s56, 8
	s_sub_i32 s38, s6, s4
	s_ashr_i32 s7, s50, 6
	s_lshl_b64 s[4:5], s[42:43], 13
	s_ashr_i32 s39, s51, 31
	s_add_u32 s4, s4, s51
	s_addc_u32 s5, s5, s39
	s_lshl_b32 s39, s7, 5
	s_ashr_i32 s40, s39, 31
	s_add_u32 s44, s4, s39
	s_addc_u32 s45, s5, s40
	s_lshl_b64 s[4:5], s[44:45], 10
	s_add_u32 s40, s8, s4
	s_addc_u32 s41, s9, s5
	s_lshl_b32 s4, s38, 6
	s_ashr_i32 s5, s4, 31
	s_lshl_b64 s[38:39], s[4:5], 1
	s_add_u32 s40, s40, s38
	s_addc_u32 s41, s41, s39
	s_lshl_b64 s[4:5], s[42:43], 23
	s_add_u32 s43, s17, s4
	s_addc_u32 s47, s18, s5
	s_add_u32 s46, s43, s38
	s_addc_u32 s47, s47, s39
	s_add_u32 s4, s19, s4
	v_and_b32_e32 v1, 63, v58
	s_addc_u32 s5, s20, s5
	s_add_u32 s48, s4, s38
	v_lshlrev_b32_e32 v2, 10, v1
	s_addc_u32 s49, s5, s39
	v_lshl_add_u64 v[4:5], s[46:47], 0, v[2:3]
	s_lshl_b32 s46, s7, 3
	s_lshl_b32 s4, s7, 4
	v_bfe_u32 v2, v58, 2, 4
	s_ashr_i32 s47, s46, 31
	v_and_or_b32 v2, s4, 48, v2
	s_ashr_i32 s4, s50, 3
	v_lshl_add_u64 v[194:195], s[46:47], 1, v[4:5]
	s_and_b32 s46, s4, 0xffffffe0
	s_and_b32 s5, s50, 0x3fffffc0
	s_ashr_i32 s47, s46, 31
	s_lshl_b32 s58, s7, 10
	s_cmp_lg_u32 0, -1
	s_cselect_b32 s4, 0, 0
	s_lshl_b32 s42, s42, 8
	s_lshl_b32 s43, s56, 3
	s_add_i32 s42, s42, s43
	s_add_i32 s42, s42, s7
	v_lshlrev_b32_e32 v2, 10, v2
	v_lshlrev_b32_e32 v212, 3, v58
	s_add_i32 s58, s58, s4
	s_ashr_i32 s43, s42, 31
	v_lshl_add_u64 v[4:5], s[48:49], 0, v[2:3]
	v_and_b32_e32 v215, 24, v212
	s_add_i32 s59, s58, 0x6000
	s_add_i32 s4, s51, 0x100
	s_lshl_b64 s[42:43], s[42:43], 15
	v_lshl_add_u64 v[4:5], s[46:47], 1, v[4:5]
	v_lshlrev_b32_e32 v2, 1, v215
	s_add_u32 s42, s23, s42
	v_lshl_add_u64 v[208:209], v[4:5], 0, v[2:3]
	s_addc_u32 s43, s54, s43
	v_lshlrev_b32_e32 v2, 2, v1
	v_lshl_add_u64 v[84:85], s[42:43], 0, v[2:3]
	global_load_dword v59, v[84:85], off
	s_waitcnt vmcnt(0)
	v_lshlrev_b32_sdwa v225, s32, v59 dst_sel:DWORD dst_unused:UNUSED_PAD src0_sel:DWORD src1_sel:BYTE_0
	v_lshlrev_b32_sdwa v226, s32, v59 dst_sel:DWORD dst_unused:UNUSED_PAD src0_sel:DWORD src1_sel:BYTE_1
	v_lshlrev_b32_sdwa v248, s32, v59 dst_sel:DWORD dst_unused:UNUSED_PAD src0_sel:DWORD src1_sel:BYTE_2
	v_lshlrev_b32_sdwa v249, s32, v59 dst_sel:DWORD dst_unused:UNUSED_PAD src0_sel:DWORD src1_sel:BYTE_3
	v_lshl_add_u64 v[186:187], v[84:85], 0, s[30:31]
	global_load_dword v218, v[186:187], off
	v_and_b32_e32 v213, 31, v58
	s_mov_b32 m0, s58
	s_nop 0
	global_load_lds_dwordx4 v[194:195], off
	v_bfe_u32 v214, v58, 5, 1
	s_mov_b32 m0, s59
	s_nop 0
	global_load_lds_dwordx4 v[208:209], off
	v_lshlrev_b32_e32 v2, 10, v213
	v_lshl_add_u64 v[4:5], v[194:195], 0, s[36:37]
	s_add_i32 s42, s58, 0x2000
	s_mov_b32 m0, s42
	s_nop 0
	global_load_lds_dwordx4 v[4:5], off
	v_lshl_or_b32 v2, v214, 4, v2
	global_load_dwordx4 v[138:141], v2, s[40:41]
	global_load_dwordx4 v[134:137], v2, s[40:41] offset:32
	global_load_dwordx4 v[126:129], v2, s[40:41] offset:64
	global_load_dwordx4 v[122:125], v2, s[40:41] offset:96
	v_mov_b32_e32 v228, 0
	v_mov_b32_e32 v229, 0
	v_mov_b32_e32 v230, 0
	v_mov_b32_e32 v231, 0
	v_mov_b32_e32 v232, 0
	v_mov_b32_e32 v233, 0
	v_mov_b32_e32 v234, 0
	v_mov_b32_e32 v235, 0
	v_mov_b32_e32 v236, 0
	v_mov_b32_e32 v237, 0
	v_mov_b32_e32 v238, 0
	v_mov_b32_e32 v239, 0
	v_mov_b32_e32 v240, 0
	v_mov_b32_e32 v241, 0
	v_mov_b32_e32 v242, 0
	v_mov_b32_e32 v243, 0
	v_mov_b32_e32 v16, v3
	v_mov_b32_e32 v17, v3
	v_lshlrev_b32_e32 v2, 10, v214
	v_lshlrev_b32_e32 v18, 4, v213
	v_mov_b32_e32 v4, v3
	v_mov_b32_e32 v5, v3
	v_mov_b32_e32 v6, v3
	v_mov_b32_e32 v7, v3
	v_mov_b32_e32 v8, v3
	v_mov_b32_e32 v9, v3
	v_mov_b32_e32 v10, v3
	v_mov_b32_e32 v11, v3
	v_mov_b32_e32 v12, v3
	v_mov_b32_e32 v13, v3
	v_mov_b32_e32 v14, v3
	v_mov_b32_e32 v15, v3
	v_add3_u32 v221, 0, v2, v18
	v_mov_b32_e32 v2, v3
	v_mov_b64_e32 v[32:33], v[16:17]
	v_mov_b64_e32 v[30:31], v[14:15]
	v_mov_b64_e32 v[28:29], v[12:13]
	v_mov_b64_e32 v[26:27], v[10:11]
	v_mov_b64_e32 v[24:25], v[8:9]
	v_mov_b64_e32 v[22:23], v[6:7]
	v_mov_b64_e32 v[20:21], v[4:5]
	v_mov_b64_e32 v[18:19], v[2:3]
	v_lshl_add_u64 v[34:35], v[194:195], 0, s[0:1]
	s_add_i32 s40, s58, 0x4000
	s_mov_b32 m0, s40
	s_nop 0
	global_load_lds_dwordx4 v[34:35], off
	s_waitcnt vmcnt(3) lgkmcnt(0)
	s_barrier
; #define MASK1(p,w,e) ({ unsigned m_; asm("v_bfe_i32 %0, %1, %2, 1":"=v"(m_):"v"(w),"n"(e)); __uint_as_float(__float_as_uint(p)&m_); })
; #define WAIT_BAR(N) asm volatile("s_waitcnt vmcnt(" #N ") lgkmcnt(0)\n\ts_barrier":::"memory")
;   #define DMA_K(t,slot) glds16(ksrc+(long)(t)*KVBLK*DM,(unsigned)__builtin_amdgcn_readfirstlane(kdst+(slot)))
; template<int THRL> __device__ __forceinline__ void attn_unit(int b,int h,int qb,const bf16*Q,const bf16*__restrict__ K,const bf16*__restrict__ V,bf16*O,const unsigned*MASK,char*shm){
;     ...
;   f32x16 pA0,pA1,pB0,pB1;
;   int sl_prev=0,sl_cur=0,sl_next=SLOTB;
;     ...
;   DMA_K(2,2*SLOTB);
;   WAIT_BAR(3);
;   qkt(pA0,pA1,Kbase,qr,negm,r32,hi);asm volatile("s_nop 15\n\ts_nop 7":"+v"(pA0),"+v"(pA1));
;   START(pA0,pA1);
;   _Pragma("unroll") for(int r=0;r<16;++r)pA1[r]=__builtin_amdgcn_exp2f(pA1[r]);
;   _Pragma("unroll") for(int r=0;r<16;++r){pA0[r]=MASK1(pA0[r],wA,r);pA1[r]=MASK1(pA1[r],wA,16+r);}
;   WAIT_BAR(0);
	ds_read_b128 v[50:53], v221
	ds_read_b128 v[54:57], v221 offset:512
	s_mov_b32 s40, 0xf149f2ca
	s_waitcnt vmcnt(3) lgkmcnt(1)
	v_mfma_f32_32x32x16_bf16 v[34:49], v[50:53], v[138:141], v[18:33]
	v_bfe_i32 v70, v59, 3, 1
	v_bfe_i32 v71, v59, 4, 1
	v_bfe_i32 v72, v59, 5, 1
	v_bfe_i32 v73, v59, 6, 1
	v_bfe_i32 v74, v59, 7, 1
	v_bfe_i32 v75, v59, 8, 1
	v_bfe_i32 v76, v59, 9, 1
	s_waitcnt lgkmcnt(0)
	v_mfma_f32_32x32x16_bf16 v[18:33], v[54:57], v[138:141], v[18:33]
	ds_read_b128 v[50:53], v221 offset:2048
	ds_read_b128 v[54:57], v221 offset:2560
	v_bfe_i32 v77, v59, 10, 1
	v_bfe_i32 v78, v59, 11, 1
	v_bfe_i32 v79, v59, 12, 1
	v_bfe_i32 v80, v59, 13, 1
	v_bfe_i32 v81, v59, 14, 1
	v_bfe_i32 v82, v59, 15, 1
	s_waitcnt vmcnt(2) lgkmcnt(1)
	v_mfma_f32_32x32x16_bf16 v[34:49], v[50:53], v[134:137], v[34:49]
	s_lshl_b32 s5, s5, 2
	v_bfe_i32 v86, v59, 16, 1
	v_bfe_i32 v87, v59, 17, 1
	v_bfe_i32 v69, v59, 2, 1
	s_ashr_i32 s61, s4, 6
	s_add_i32 s57, s5, 0
	v_bfe_i32 v67, v59, 0, 1
	s_waitcnt lgkmcnt(0)
	v_mfma_f32_32x32x16_bf16 v[18:33], v[54:57], v[134:137], v[18:33]
	ds_read_b128 v[50:53], v221 offset:4096
	ds_read_b128 v[54:57], v221 offset:4608
	v_bfe_i32 v68, v59, 1, 1
	s_mov_b32 s92, 1
	s_mov_b32 s48, 0
	s_movk_i32 s60, 0x2000
	s_movk_i32 s62, 0x4000
	v_bfe_i32 v88, v59, 18, 1
	s_waitcnt vmcnt(1) lgkmcnt(1)
	v_mfma_f32_32x32x16_bf16 v[34:49], v[50:53], v[126:129], v[34:49]
	ds_read_b128 v[50:53], v221 offset:6144
	v_bfe_i32 v89, v59, 19, 1
	v_bfe_i32 v90, v59, 20, 1
	v_bfe_i32 v91, v59, 21, 1
	v_bfe_i32 v92, v59, 22, 1
	v_bfe_i32 v93, v59, 23, 1
	v_bfe_i32 v94, v59, 24, 1
	s_waitcnt lgkmcnt(1)
	v_mfma_f32_32x32x16_bf16 v[18:33], v[54:57], v[126:129], v[18:33]
	ds_read_b128 v[54:57], v221 offset:6656
	v_bfe_i32 v95, v59, 25, 1
	v_bfe_i32 v96, v59, 26, 1
	v_bfe_i32 v97, v59, 27, 1
	v_bfe_i32 v98, v59, 28, 1
	v_bfe_i32 v99, v59, 29, 1
	v_bfe_i32 v100, v59, 30, 1
	s_waitcnt vmcnt(0) lgkmcnt(1)
	v_mfma_f32_32x32x16_bf16 v[34:49], v[50:53], v[122:125], v[34:49]
	v_lshlrev_b32_e32 v50, 1, v58
	v_lshlrev_b32_e32 v51, 4, v58
	v_and_b32_e32 v217, 32, v50
	v_and_b32_e32 v50, 0xc0, v51
	v_lshl_or_b32 v216, v214, 8, v50
	v_add_u32_e32 v50, 0, v217
	v_add3_u32 v220, v50, v215, v216
	s_waitcnt lgkmcnt(0)
	v_mfma_f32_32x32x16_bf16 v[18:33], v[54:57], v[122:125], v[18:33]
	s_nop 15
	s_nop 7
	s_nop 0
	v_max3_f32 v50, v34, v35, v18
	v_max3_f32 v51, v36, v37, v19
	s_nop 0
	v_max3_f32 v50, v50, v20, v21
	v_max3_f32 v51, v51, v40, v41
	s_nop 0
	v_max3_f32 v50, v50, v38, v39
	v_max3_f32 v51, v51, v24, v25
	s_nop 0
	v_max3_f32 v50, v50, v22, v23
	v_max3_f32 v51, v51, v44, v45
	s_nop 0
	v_max3_f32 v50, v50, v42, v43
	v_max3_f32 v51, v51, v28, v29
	s_nop 0
	v_max3_f32 v50, v50, v26, v27
	v_max3_f32 v51, v51, v48, v49
	s_nop 0
	v_max3_f32 v50, v50, v46, v47
	v_max3_f32 v51, v51, v32, v33
	s_nop 0
	v_max3_f32 v50, v50, v30, v31
	s_nop 0
	v_max_f32_e32 v50, v50, v51
	s_nop 0
	v_mov_b32_e32 v51, v50
	s_nop 1
	v_permlane32_swap_b32_e32 v50, v51
	v_max_f32_e32 v50, v50, v51
	s_nop 0
	v_cmp_lt_f32_e32 vcc, s40, v50
	v_cmp_gt_u32_e64 s[40:41], 32, v1
	s_nop 0
	v_cndmask_b32_e32 v50, 0, v50, vcc
	v_sub_f32_e32 v18, v18, v50
	v_sub_f32_e32 v19, v19, v50
	v_sub_f32_e32 v52, v36, v50
	v_sub_f32_e32 v53, v37, v50
	v_sub_f32_e32 v54, v38, v50
	v_sub_f32_e32 v55, v39, v50
	v_sub_f32_e32 v56, v40, v50
	v_sub_f32_e32 v57, v41, v50
	v_sub_f32_e32 v58, v42, v50
	v_sub_f32_e32 v60, v43, v50
	v_sub_f32_e32 v61, v44, v50
	v_sub_f32_e32 v62, v45, v50
	v_sub_f32_e32 v63, v46, v50
	v_sub_f32_e32 v64, v47, v50
	v_sub_f32_e32 v65, v48, v50
	v_sub_f32_e32 v66, v49, v50
	s_nop 0
	v_exp_f32_e32 v52, v52
	v_exp_f32_e32 v53, v53
	v_exp_f32_e32 v54, v54
	v_exp_f32_e32 v55, v55
	v_exp_f32_e32 v56, v56
	v_exp_f32_e32 v57, v57
	v_exp_f32_e32 v58, v58
	v_exp_f32_e32 v60, v60
	v_exp_f32_e32 v61, v61
	v_exp_f32_e32 v62, v62
	v_exp_f32_e32 v63, v63
	v_exp_f32_e32 v64, v64
	v_exp_f32_e32 v65, v65
	v_exp_f32_e32 v66, v66
	v_exp_f32_e32 v18, v18
	v_exp_f32_e32 v19, v19
	v_add_f32_e32 v219, v3, v50
	v_sub_f32_e32 v34, v34, v50
	v_sub_f32_e32 v35, v35, v50
	v_sub_f32_e32 v20, v20, v50
	v_sub_f32_e32 v21, v21, v50
	v_sub_f32_e32 v22, v22, v50
	s_nop 0
	v_xor_b32_e32 v36, 0x80000000, v219
	v_sub_f32_e32 v23, v23, v50
	v_sub_f32_e32 v24, v24, v50
	v_sub_f32_e32 v25, v25, v50
	v_sub_f32_e32 v26, v26, v50
	v_sub_f32_e32 v27, v27, v50
	v_sub_f32_e32 v28, v28, v50
	v_sub_f32_e32 v29, v29, v50
	v_sub_f32_e32 v30, v30, v50
	v_sub_f32_e32 v31, v31, v50
	v_sub_f32_e32 v32, v32, v50
	v_sub_f32_e32 v33, v33, v50
	v_mov_b32_e32 v37, v36
	v_mov_b32_e32 v38, v36
	v_mov_b32_e32 v39, v36
	v_mov_b32_e32 v40, v36
	v_mov_b32_e32 v41, v36
	v_mov_b32_e32 v42, v36
	v_mov_b32_e32 v43, v36
	v_mov_b32_e32 v44, v36
	v_mov_b32_e32 v45, v36
	v_mov_b32_e32 v46, v36
	v_mov_b32_e32 v47, v36
	v_mov_b32_e32 v48, v36
	v_mov_b32_e32 v49, v36
	v_mov_b32_e32 v50, v36
	v_mov_b32_e32 v51, v36
	s_waitcnt vmcnt(0) lgkmcnt(0)
	s_barrier
; #define MASK1(p,w,e) ({ unsigned m_; asm("v_bfe_i32 %0, %1, %2, 1":"=v"(m_):"v"(w),"n"(e)); __uint_as_float(__float_as_uint(p)&m_); })
; #define WAIT_BAR(N) asm volatile("s_waitcnt vmcnt(" #N ") lgkmcnt(0)\n\ts_barrier":::"memory")
;   #define DMA_K(t,slot) glds16(ksrc+(long)(t)*KVBLK*DM,(unsigned)__builtin_amdgcn_readfirstlane(kdst+(slot)))
;   #define DMA_V(t,slot) glds16(vsrc+(long)(t)*KVBLK*DM,(unsigned)__builtin_amdgcn_readfirstlane(vdst+(slot)))
;   #define ROT() do{sl_prev=sl_cur;sl_cur=sl_next;sl_next=(sl_next==(NSLOT-1)*SLOTB)?0:sl_next+SLOTB;}while(0)
; template<int THRL> __device__ __forceinline__ void attn_unit(int b,int h,int qb,const bf16*Q,const bf16*__restrict__ K,const bf16*__restrict__ V,bf16*O,const unsigned*MASK,char*shm){
;     ...
;   _Pragma("unroll") for(int r=0;r<16;++r){pA0[r]=MASK1(pA0[r],wA,r);pA1[r]=MASK1(pA1[r],wA,16+r);}
;   WAIT_BAR(0);
;   DMA_K(3,0);DMA_V(1,SLOTB);
;   ROT();
;   kload8(kf,kp0+sl_cur);
;   WAIT_BAR(2);
;   s16x4 vlo[8],vhi[8]; u32x4 pw0,pw1,pw2,pw3;
	v_and_b32_e32 v83, v82, v66
	v_and_b32_e32 v82, v81, v65
	v_and_b32_e32 v81, v80, v64
	v_and_b32_e32 v80, v79, v63
	v_and_b32_e32 v79, v78, v62
	v_and_b32_e32 v78, v77, v61
	v_and_b32_e32 v77, v76, v60
	v_and_b32_e32 v76, v75, v58
	v_and_b32_e32 v75, v74, v57
	v_and_b32_e32 v74, v73, v56
	v_and_b32_e32 v73, v72, v55
	v_and_b32_e32 v72, v71, v54
	v_and_b32_e32 v71, v70, v53
	v_and_b32_e32 v70, v69, v52
	v_and_b32_e32 v53, v87, v19
	v_and_b32_e32 v52, v86, v18
	v_lshl_add_u64 v[18:19], v[194:195], 0, s[82:83]
	s_mov_b32 m0, s58
	s_nop 0
	global_load_lds_dwordx4 v[18:19], off
	v_lshl_add_u64 v[18:19], v[208:209], 0, s[36:37]
	s_add_i32 s4, s58, 0x8000
	s_mov_b32 m0, s4
	s_nop 0
	global_load_lds_dwordx4 v[18:19], off
	ds_read_b128 v[178:181], v221 offset:8192
	ds_read_b128 v[170:173], v221 offset:8704
	ds_read_b128 v[174:177], v221 offset:10240
	ds_read_b128 v[162:165], v221 offset:10752
	ds_read_b128 v[166:169], v221 offset:12288
	ds_read_b128 v[154:157], v221 offset:12800
	ds_read_b128 v[158:161], v221 offset:14336
	ds_read_b128 v[150:153], v221 offset:14848
	v_exp_f32_e32 v34, v34
	v_exp_f32_e32 v35, v35
	v_exp_f32_e32 v20, v20
	v_exp_f32_e32 v21, v21
	v_exp_f32_e32 v22, v22
	v_exp_f32_e32 v23, v23
	v_exp_f32_e32 v24, v24
	v_exp_f32_e32 v25, v25
	v_exp_f32_e32 v26, v26
	v_exp_f32_e32 v27, v27
	v_exp_f32_e32 v28, v28
	v_exp_f32_e32 v29, v29
	v_exp_f32_e32 v30, v30
	v_exp_f32_e32 v31, v31
	v_exp_f32_e32 v32, v32
	v_exp_f32_e32 v33, v33
	s_waitcnt vmcnt(2) lgkmcnt(0)
	s_barrier
	v_and_b32_e32 v69, v68, v35
	v_and_b32_e32 v68, v67, v34
	v_bfe_i32 v34, v59, 31, 1
	v_and_b32_e32 v66, v100, v32
	v_and_b32_e32 v67, v34, v33
	v_and_b32_e32 v65, v99, v31
	v_and_b32_e32 v64, v98, v30
	v_and_b32_e32 v63, v97, v29
	v_and_b32_e32 v62, v96, v28
	v_and_b32_e32 v61, v95, v27
	v_and_b32_e32 v60, v94, v26
	v_and_b32_e32 v59, v93, v25
	v_and_b32_e32 v58, v92, v24
	v_and_b32_e32 v57, v91, v23
	v_and_b32_e32 v56, v90, v22
	v_and_b32_e32 v55, v89, v21
	v_and_b32_e32 v54, v88, v20
	s_cmp_lt_i32 s61, 7
	s_cbranch_scc1 .LBB0_1287
	s_mov_b64 s[4:5], 0x50000
	v_lshlrev_b32_e32 v18, 4, v214
	v_lshl_add_u64 v[188:189], v[194:195], 0, s[4:5]
	s_mov_b64 s[4:5], 0x300
	v_mov_b64_e32 v[34:35], v[16:17]
	v_lshl_add_u64 v[192:193], v[84:85], 0, s[4:5]
	v_add_u32_e32 v85, s57, v18
	v_mov_b64_e32 v[32:33], v[14:15]
	v_mov_b64_e32 v[30:31], v[12:13]
	v_mov_b64_e32 v[28:29], v[10:11]
	v_mov_b64_e32 v[26:27], v[8:9]
	v_mov_b64_e32 v[24:25], v[6:7]
	v_mov_b64_e32 v[22:23], v[4:5]
	v_mov_b64_e32 v[20:21], v[2:3]
	v_mov_b64_e32 v[18:19], v[16:17]
	s_add_i32 s46, s61, -5
	v_lshl_add_u32 v210, v213, 2, s57
	v_lshl_add_u64 v[190:191], v[208:209], 0, s[82:83]
	s_mov_b32 s4, 0
	s_movk_i32 s48, 0x4000
	s_movk_i32 s47, 0x2000
	v_mov_b32_e32 v84, 0
	v_mov_b64_e32 v[16:17], v[14:15]
	v_mov_b64_e32 v[14:15], v[12:13]
	v_mov_b64_e32 v[12:13], v[10:11]
	v_mov_b64_e32 v[10:11], v[8:9]
	v_mov_b64_e32 v[8:9], v[6:7]
	v_mov_b64_e32 v[6:7], v[4:5]
	v_mov_b64_e32 v[4:5], v[2:3]
.LBB0_1273:
	s_movk_i32 s42, 0xff00
	s_mov_b32 s43, -1
	v_lshl_add_u64 v[86:87], v[192:193], 0, s[42:43]
	global_load_dword v2, v[86:87], off
	v_add_u32_e32 v255, s4, v220
	ds_read_b64_tr_b16 v[182:183], v255 offset:24576
	ds_read_b64_tr_b16 v[184:185], v255 offset:25088
	s_waitcnt lgkmcnt(9)
	v_mfma_f32_32x32x16_bf16 v[102:117], v[178:181], v[138:141], v[36:51]
	v_cvt_pk_bf16_f32 v146, v68, v69
	v_cvt_pk_bf16_f32 v147, v70, v71
	ds_read_b64_tr_b16 v[178:179], v255 offset:28672
	ds_read_b64_tr_b16 v[180:181], v255 offset:29184
	s_waitcnt lgkmcnt(10)
	v_mfma_f32_32x32x16_bf16 v[86:101], v[170:173], v[138:141], v[36:51]
	v_cvt_pk_bf16_f32 v148, v72, v73
	v_cvt_pk_bf16_f32 v149, v74, v75
	ds_read_b64_tr_b16 v[170:171], v255 offset:25600
	ds_read_b64_tr_b16 v[172:173], v255 offset:26112
	s_waitcnt lgkmcnt(11)
	v_mfma_f32_32x32x16_bf16 v[102:117], v[174:177], v[134:137], v[102:117]
	v_cvt_pk_bf16_f32 v142, v76, v77
	v_cvt_pk_bf16_f32 v143, v78, v79
	ds_read_b64_tr_b16 v[76:77], v255 offset:29696
	ds_read_b64_tr_b16 v[78:79], v255 offset:30208
	s_waitcnt lgkmcnt(12)
	v_mfma_f32_32x32x16_bf16 v[86:101], v[162:165], v[134:137], v[86:101]
	v_cvt_pk_bf16_f32 v144, v80, v81
	v_cvt_pk_bf16_f32 v145, v82, v83
	ds_read_b64_tr_b16 v[72:73], v255 offset:26624
	ds_read_b64_tr_b16 v[74:75], v255 offset:27136
	s_waitcnt lgkmcnt(13)
	v_mfma_f32_32x32x16_bf16 v[102:117], v[166:169], v[126:129], v[102:117]
	v_cvt_pk_bf16_f32 v130, v52, v53
	v_cvt_pk_bf16_f32 v131, v54, v55
	ds_read_b64_tr_b16 v[68:69], v255 offset:30720
	ds_read_b64_tr_b16 v[70:71], v255 offset:31232
	s_waitcnt lgkmcnt(14)
	v_mfma_f32_32x32x16_bf16 v[86:101], v[154:157], v[126:129], v[86:101]
	v_cvt_pk_bf16_f32 v132, v56, v57
	v_cvt_pk_bf16_f32 v133, v58, v59
	ds_read_b64_tr_b16 v[56:57], v255 offset:27648
	ds_read_b64_tr_b16 v[58:59], v255 offset:28160
	s_waitcnt lgkmcnt(14)
	v_mfma_f32_32x32x16_bf16 v[102:117], v[158:161], v[122:125], v[102:117]
	v_cvt_pk_bf16_f32 v118, v60, v61
	v_cvt_pk_bf16_f32 v119, v62, v63
	ds_read_b64_tr_b16 v[52:53], v255 offset:31744
	ds_read_b64_tr_b16 v[54:55], v255 offset:32256
	v_mfma_f32_32x32x16_bf16 v[86:101], v[150:153], v[122:125], v[86:101]
	v_cvt_pk_bf16_f32 v120, v64, v65
	v_cvt_pk_bf16_f32 v121, v66, v67
	ds_read_b128 v[80:83], v225 offset:51200
	v_lshl_add_u64 v[60:61], v[188:189], 0, s[86:87]
	s_add_i32 s4, s47, s58
	s_mov_b32 m0, s4
	s_nop 0
	global_load_lds_dwordx4 v[60:61], off
	v_lshl_add_u64 v[60:61], v[190:191], 0, s[86:87]
	s_add_i32 s4, s48, s59
	s_mov_b32 m0, s4
	s_nop 0
	global_load_lds_dwordx4 v[60:61], off
	v_max_f32_e32 v60, v103, v103
	v_max_f32_e32 v61, v102, v102
	v_max_f32_e32 v60, v61, v60
	v_max3_f32 v61, v104, v105, v87
	v_max3_f32 v60, v60, v86, v88
	v_max3_f32 v60, v60, v89, v106
	v_max3_f32 v61, v61, v108, v109
	v_max3_f32 v60, v60, v107, v90
	v_max3_f32 v61, v61, v92, v93
	v_max3_f32 v60, v60, v91, v110
	v_max3_f32 v61, v61, v112, v113
	v_max3_f32 v60, v60, v111, v94
	v_max3_f32 v61, v61, v96, v97
	v_max3_f32 v60, v60, v95, v114
	v_max3_f32 v61, v61, v116, v117
	v_max3_f32 v60, v60, v115, v98
	v_max3_f32 v61, v61, v100, v101
	v_max3_f32 v60, v60, v99, v61
	v_mov_b32_e32 v61, v60
	s_nop 1
	v_permlane32_swap_b32_e32 v60, v61
	v_max_f32_e32 v61, v61, v61
	v_max_f32_e32 v60, v60, v60
	v_max_f32_e32 v60, v60, v61
	v_cmp_lt_f32_e32 vcc, s14, v60
	s_cmp_lg_u64 vcc, 0
	s_cselect_b64 s[42:43], -1, 0
	s_cbranch_vccnz .LBB0_1281

.LBB0_1276:
	s_add_i32 s4, s48, 0x2000
	s_cmpk_lg_i32 s48, 0x4000
	s_cselect_b32 s60, s4, 0
	global_load_dword v218, v[192:193], off
	v_add_u32_e32 v255, s47, v220
	ds_read_b64_tr_b16 v[182:183], v255 offset:24576
	ds_read_b64_tr_b16 v[184:185], v255 offset:25088
	s_waitcnt lgkmcnt(9)
	v_mfma_f32_32x32x16_bf16 v[68:83], v[60:63], v[138:141], v[36:51]
	v_cvt_pk_bf16_f32 v146, v102, v103
	v_cvt_pk_bf16_f32 v147, v104, v105
	ds_read_b64_tr_b16 v[178:179], v255 offset:28672
	ds_read_b64_tr_b16 v[180:181], v255 offset:29184
	s_waitcnt lgkmcnt(10)
	v_mfma_f32_32x32x16_bf16 v[52:67], v[150:153], v[138:141], v[36:51]
	v_cvt_pk_bf16_f32 v148, v106, v107
	v_cvt_pk_bf16_f32 v149, v108, v109
	ds_read_b64_tr_b16 v[150:151], v255 offset:25600
	ds_read_b64_tr_b16 v[152:153], v255 offset:26112
	s_waitcnt lgkmcnt(11)
	v_mfma_f32_32x32x16_bf16 v[68:83], v[174:177], v[134:137], v[68:83]
	v_cvt_pk_bf16_f32 v142, v110, v111
	v_cvt_pk_bf16_f32 v143, v112, v113
	ds_read_b64_tr_b16 v[110:111], v255 offset:29696
	ds_read_b64_tr_b16 v[112:113], v255 offset:30208
	s_waitcnt lgkmcnt(12)
	v_mfma_f32_32x32x16_bf16 v[52:67], v[162:165], v[134:137], v[52:67]
	v_cvt_pk_bf16_f32 v144, v114, v115
	v_cvt_pk_bf16_f32 v145, v116, v117
	ds_read_b64_tr_b16 v[106:107], v255 offset:26624
	ds_read_b64_tr_b16 v[108:109], v255 offset:27136
	s_waitcnt lgkmcnt(13)
	v_mfma_f32_32x32x16_bf16 v[68:83], v[170:173], v[126:129], v[68:83]
	v_cvt_pk_bf16_f32 v130, v86, v87
	v_cvt_pk_bf16_f32 v131, v88, v89
	ds_read_b64_tr_b16 v[102:103], v255 offset:30720
	ds_read_b64_tr_b16 v[104:105], v255 offset:31232
	s_waitcnt lgkmcnt(14)
	v_mfma_f32_32x32x16_bf16 v[52:67], v[158:161], v[126:129], v[52:67]
	v_cvt_pk_bf16_f32 v132, v90, v91
	v_cvt_pk_bf16_f32 v133, v92, v93
	ds_read_b64_tr_b16 v[90:91], v255 offset:27648
	ds_read_b64_tr_b16 v[92:93], v255 offset:28160
	s_waitcnt lgkmcnt(14)
	v_mfma_f32_32x32x16_bf16 v[68:83], v[166:169], v[122:125], v[68:83]
	v_cvt_pk_bf16_f32 v118, v94, v95
	v_cvt_pk_bf16_f32 v119, v96, v97
	ds_read_b64_tr_b16 v[86:87], v255 offset:31744
	ds_read_b64_tr_b16 v[88:89], v255 offset:32256
	v_mfma_f32_32x32x16_bf16 v[52:67], v[154:157], v[122:125], v[52:67]
	v_cvt_pk_bf16_f32 v120, v98, v99
	v_cvt_pk_bf16_f32 v121, v100, v101
	ds_read_b128 v[114:117], v225 offset:51200
	v_max_f32_e32 v95, v69, v69
	v_max_f32_e32 v96, v68, v68
	v_max_f32_e32 v95, v96, v95
	s_nop 3
	v_max3_f32 v96, v70, v71, v53
	v_max3_f32 v95, v95, v52, v54
	v_max3_f32 v95, v95, v55, v72
	v_max3_f32 v96, v96, v74, v75
	v_max3_f32 v95, v95, v73, v56
	v_max3_f32 v96, v96, v58, v59
	v_max3_f32 v95, v95, v57, v76
	v_max3_f32 v96, v96, v78, v79
	v_max3_f32 v95, v95, v77, v60
	v_max3_f32 v96, v96, v62, v63
	v_max3_f32 v95, v95, v61, v80
	v_max3_f32 v96, v96, v82, v83
	v_max3_f32 v95, v95, v81, v64
	v_max3_f32 v96, v96, v66, v67
	v_max3_f32 v94, v95, v65, v96
	v_mov_b32_e32 v95, v94
	s_nop 1
	v_permlane32_swap_b32_e32 v94, v95
	v_max_f32_e32 v95, v95, v95
	v_max_f32_e32 v94, v94, v94
	s_add_i32 s4, s48, s58
	s_mov_b32 m0, s4
	s_nop 0
	global_load_lds_dwordx4 v[188:189], off
	v_max_f32_e32 v94, v94, v95
	s_add_i32 s4, s60, s59
	s_mov_b32 m0, s4
	s_nop 0
	global_load_lds_dwordx4 v[190:191], off
	v_cmp_lt_f32_e32 vcc, s14, v94
	s_cmp_lg_u64 vcc, 0
	s_cselect_b64 s[42:43], -1, 0
	s_cbranch_vccnz .LBB0_1284

;   #define RESC() do{ if(resc){ asm volatile("s_waitcnt lgkmcnt(0)":::"memory"); \
;       _Pragma("unroll") for(int d_=0;d_<2;++d_) _Pragma("unroll") for(int r=0;r<16;++r)o[d_][r]*=wsf[crow(r,hi)]; } }while(0)
;   #define ROT() do{sl_prev=sl_cur;sl_cur=sl_next;sl_next=(sl_next==(NSLOT-1)*SLOTB)?0:sl_next+SLOTB;}while(0)
;   #define ENDW(tt) do{ if((tt)+3<NT){WAIT_BAR(2);} else if((tt)+2<NT){WAIT_BAR(1);} else {WAIT_BAR(0);} }while(0)
; template<int THRL> __device__ __forceinline__ void attn_unit(int b,int h,int qb,const bf16*Q,const bf16*__restrict__ K,const bf16*__restrict__ V,bf16*O,const unsigned*MASK,char*shm){
;     ...
;   for(;t+1<NT;t+=2){
;     STEP(pB0,pB1,pA0,pA1,t,(t+3<NT),(t+1<NT),(t+1<NT),wB,wA);       ENDW(t);   RESC(); ROT();
;     STEP(pA0,pA1,pB0,pB1,t+1,(t+4<NT),(t+2<NT),(t+2<NT),wA,wB);     ENDW(t+1); RESC(); ROT();
.LBB0_1290:
	global_load_dword v223, v[210:211], off
	v_add_u32_e32 v85, s48, v220
	ds_read_b64_tr_b16 v[186:187], v85 offset:24576
	ds_read_b64_tr_b16 v[188:189], v85 offset:25088
	s_waitcnt lgkmcnt(9)
	v_mfma_f32_32x32x16_bf16 v[102:117], v[178:181], v[138:141], v[36:51]
	v_cvt_pk_bf16_f32 v146, v68, v69
	v_cvt_pk_bf16_f32 v147, v70, v71
	ds_read_b64_tr_b16 v[178:179], v85 offset:28672
	ds_read_b64_tr_b16 v[180:181], v85 offset:29184
	s_waitcnt lgkmcnt(10)
	v_mfma_f32_32x32x16_bf16 v[86:101], v[170:173], v[138:141], v[36:51]
	v_cvt_pk_bf16_f32 v148, v72, v73
	v_cvt_pk_bf16_f32 v149, v74, v75
	ds_read_b64_tr_b16 v[182:183], v85 offset:25600
	ds_read_b64_tr_b16 v[184:185], v85 offset:26112
	s_waitcnt lgkmcnt(11)
	v_mfma_f32_32x32x16_bf16 v[102:117], v[174:177], v[134:137], v[102:117]
	v_cvt_pk_bf16_f32 v142, v76, v77
	v_cvt_pk_bf16_f32 v143, v78, v79
	ds_read_b64_tr_b16 v[76:77], v85 offset:29696
	ds_read_b64_tr_b16 v[78:79], v85 offset:30208
	s_waitcnt lgkmcnt(12)
	v_mfma_f32_32x32x16_bf16 v[86:101], v[162:165], v[134:137], v[86:101]
	v_cvt_pk_bf16_f32 v144, v80, v81
	v_cvt_pk_bf16_f32 v145, v82, v83
	ds_read_b64_tr_b16 v[72:73], v85 offset:26624
	ds_read_b64_tr_b16 v[74:75], v85 offset:27136
	s_waitcnt lgkmcnt(13)
	v_mfma_f32_32x32x16_bf16 v[102:117], v[166:169], v[126:129], v[102:117]
	v_cvt_pk_bf16_f32 v130, v52, v53
	v_cvt_pk_bf16_f32 v131, v54, v55
	ds_read_b64_tr_b16 v[68:69], v85 offset:30720
	ds_read_b64_tr_b16 v[70:71], v85 offset:31232
	s_waitcnt lgkmcnt(14)
	v_mfma_f32_32x32x16_bf16 v[86:101], v[154:157], v[126:129], v[86:101]
	v_cvt_pk_bf16_f32 v132, v56, v57
	v_cvt_pk_bf16_f32 v133, v58, v59
	ds_read_b64_tr_b16 v[56:57], v85 offset:27648
	ds_read_b64_tr_b16 v[58:59], v85 offset:28160
	s_waitcnt lgkmcnt(14)
	v_mfma_f32_32x32x16_bf16 v[102:117], v[158:161], v[122:125], v[102:117]
	v_cvt_pk_bf16_f32 v118, v60, v61
	v_cvt_pk_bf16_f32 v119, v62, v63
	ds_read_b64_tr_b16 v[52:53], v85 offset:31744
	ds_read_b64_tr_b16 v[54:55], v85 offset:32256
	v_mfma_f32_32x32x16_bf16 v[86:101], v[150:153], v[122:125], v[86:101]
	v_cvt_pk_bf16_f32 v120, v64, v65
	v_cvt_pk_bf16_f32 v121, v66, v67
	ds_read_b128 v[80:83], v225 offset:51200
	s_add_i32 s65, s64, -1
	s_cmp_ge_i32 s65, s61
	s_cselect_b64 s[48:49], -1, 0
	s_and_b64 vcc, exec, s[48:49]
	s_cbranch_vccnz .LBB0_1292
	v_lshl_add_u64 v[62:63], v[194:195], 0, s[46:47]
	s_add_i32 s4, s60, s58
	v_lshl_add_u64 v[62:63], v[62:63], 0, s[82:83]
	s_mov_b32 m0, s4
	s_nop 0
	global_load_lds_dwordx4 v[62:63], off
.LBB0_1292:
	v_lshl_add_u64 v[84:85], v[208:209], 0, s[46:47]
	v_lshl_add_u64 v[60:61], v[84:85], 0, s[36:37]
	s_add_i32 s4, s62, s59
	s_mov_b32 m0, s4
	s_nop 0
	global_load_lds_dwordx4 v[60:61], off
	v_max_f32_e32 v60, v103, v103
	v_max_f32_e32 v61, v102, v102
	v_max_f32_e32 v60, v61, v60
	v_max3_f32 v61, v104, v105, v87
	v_max3_f32 v60, v60, v86, v88
	v_max3_f32 v60, v60, v89, v106
	v_max3_f32 v61, v61, v108, v109
	v_max3_f32 v60, v60, v107, v90
	v_max3_f32 v61, v61, v92, v93
	v_max3_f32 v60, v60, v91, v110
	v_max3_f32 v61, v61, v112, v113
	v_max3_f32 v60, v60, v111, v94
	v_max3_f32 v61, v61, v96, v97
	v_max3_f32 v60, v60, v95, v114
	v_max3_f32 v61, v61, v116, v117
	v_max3_f32 v60, v60, v115, v98
	v_max3_f32 v61, v61, v100, v101
	v_max3_f32 v60, v60, v99, v61
	v_mov_b32_e32 v61, v60
	s_nop 1
	v_permlane32_swap_b32_e32 v60, v61
	v_max_f32_e32 v61, v61, v61
	v_max_f32_e32 v60, v60, v60
	v_max_f32_e32 v60, v60, v61
	v_cmp_lt_f32_e32 vcc, s14, v60
	s_cmp_lg_u64 vcc, 0
	s_cselect_b64 s[42:43], -1, 0
	s_cbranch_vccnz .LBB0_1330

;   #define RESC() do{ if(resc){ asm volatile("s_waitcnt lgkmcnt(0)":::"memory"); \
;       _Pragma("unroll") for(int d_=0;d_<2;++d_) _Pragma("unroll") for(int r=0;r<16;++r)o[d_][r]*=wsf[crow(r,hi)]; } }while(0)
;   #define ROT() do{sl_prev=sl_cur;sl_cur=sl_next;sl_next=(sl_next==(NSLOT-1)*SLOTB)?0:sl_next+SLOTB;}while(0)
;   #define ENDW(tt) do{ if((tt)+3<NT){WAIT_BAR(2);} else if((tt)+2<NT){WAIT_BAR(1);} else {WAIT_BAR(0);} }while(0)
; template<int THRL> __device__ __forceinline__ void attn_unit(int b,int h,int qb,const bf16*Q,const bf16*__restrict__ K,const bf16*__restrict__ V,bf16*O,const unsigned*MASK,char*shm){
;     ...
;   for(;t+1<NT;t+=2){
;     STEP(pB0,pB1,pA0,pA1,t,(t+3<NT),(t+1<NT),(t+1<NT),wB,wA);       ENDW(t);   RESC(); ROT();
;     STEP(pA0,pA1,pB0,pB1,t+1,(t+4<NT),(t+2<NT),(t+2<NT),wA,wB);     ENDW(t+1); RESC(); ROT();
.LBB0_1299:
	v_add_u32_e32 v255, s60, v220
	ds_read_b64_tr_b16 v[190:191], v255 offset:24576
	ds_read_b64_tr_b16 v[192:193], v255 offset:25088
	s_waitcnt lgkmcnt(9)
	v_mfma_f32_32x32x16_bf16 v[68:83], v[178:181], v[138:141], v[36:51]
	v_cvt_pk_bf16_f32 v146, v102, v103
	v_cvt_pk_bf16_f32 v147, v104, v105
	ds_read_b64_tr_b16 v[186:187], v255 offset:28672
	ds_read_b64_tr_b16 v[188:189], v255 offset:29184
	s_waitcnt lgkmcnt(10)
	v_mfma_f32_32x32x16_bf16 v[52:67], v[170:173], v[138:141], v[36:51]
	v_cvt_pk_bf16_f32 v148, v106, v107
	v_cvt_pk_bf16_f32 v149, v108, v109
	ds_read_b64_tr_b16 v[182:183], v255 offset:25600
	ds_read_b64_tr_b16 v[184:185], v255 offset:26112
	s_waitcnt lgkmcnt(11)
	v_mfma_f32_32x32x16_bf16 v[68:83], v[174:177], v[134:137], v[68:83]
	v_cvt_pk_bf16_f32 v142, v110, v111
	v_cvt_pk_bf16_f32 v143, v112, v113
	ds_read_b64_tr_b16 v[110:111], v255 offset:29696
	ds_read_b64_tr_b16 v[112:113], v255 offset:30208
	s_waitcnt lgkmcnt(12)
	v_mfma_f32_32x32x16_bf16 v[52:67], v[162:165], v[134:137], v[52:67]
	v_cvt_pk_bf16_f32 v144, v114, v115
	v_cvt_pk_bf16_f32 v145, v116, v117
	ds_read_b64_tr_b16 v[106:107], v255 offset:26624
	ds_read_b64_tr_b16 v[108:109], v255 offset:27136
	s_waitcnt lgkmcnt(13)
	v_mfma_f32_32x32x16_bf16 v[68:83], v[166:169], v[126:129], v[68:83]
	v_cvt_pk_bf16_f32 v130, v86, v87
	v_cvt_pk_bf16_f32 v131, v88, v89
	ds_read_b64_tr_b16 v[102:103], v255 offset:30720
	ds_read_b64_tr_b16 v[104:105], v255 offset:31232
	s_waitcnt lgkmcnt(14)
	v_mfma_f32_32x32x16_bf16 v[52:67], v[154:157], v[126:129], v[52:67]
	v_cvt_pk_bf16_f32 v132, v90, v91
	v_cvt_pk_bf16_f32 v133, v92, v93
	ds_read_b64_tr_b16 v[90:91], v255 offset:27648
	ds_read_b64_tr_b16 v[92:93], v255 offset:28160
	s_waitcnt lgkmcnt(14)
	v_mfma_f32_32x32x16_bf16 v[68:83], v[158:161], v[122:125], v[68:83]
	v_cvt_pk_bf16_f32 v118, v94, v95
	v_cvt_pk_bf16_f32 v119, v96, v97
	ds_read_b64_tr_b16 v[86:87], v255 offset:31744
	ds_read_b64_tr_b16 v[88:89], v255 offset:32256
	v_mfma_f32_32x32x16_bf16 v[52:67], v[150:153], v[122:125], v[52:67]
	v_cvt_pk_bf16_f32 v120, v98, v99
	v_cvt_pk_bf16_f32 v121, v100, v101
	ds_read_b128 v[114:117], v225 offset:51200
	s_cmp_ge_i32 s64, s61
	s_cselect_b64 s[50:51], -1, 0
	s_and_b64 vcc, exec, s[50:51]
	s_cbranch_vccnz .LBB0_1301
	v_lshl_add_u64 v[96:97], v[194:195], 0, s[46:47]
	s_mov_b64 s[4:5], 0x40000
	s_add_i32 s42, s62, s58
	v_lshl_add_u64 v[96:97], v[96:97], 0, s[4:5]
	s_mov_b32 m0, s42
	s_nop 0
	global_load_lds_dwordx4 v[96:97], off
.LBB0_1301:
	s_add_i32 s4, s62, 0x2000
	s_cmpk_lg_i32 s62, 0x4000
	v_cndmask_b32_e64 v95, 0, 1, s[52:53]
	s_cselect_b32 s60, s4, 0
	v_cmp_ne_u32_e64 s[42:43], 1, v95
	s_andn2_b64 vcc, exec, s[52:53]
	s_cbranch_vccnz .LBB0_1303
	s_add_i32 s4, s60, s59
	v_lshl_add_u64 v[84:85], v[84:85], 0, s[0:1]
	s_mov_b32 m0, s4
	s_nop 0
	global_load_lds_dwordx4 v[84:85], off
